# 96 of the 256 workgroups convert expert weights (tiles 1152..10751) during the dense gate/up GEMM phase instead of running GEMM units; on top of v13
# speedup vs baseline: 1.0149x; 1.0040x over previous
.LBB0_364:
	v_and_b32_e32 v2, 0xfc, v200
	v_lshrrev_b32_e32 v141, 6, v0
	s_cmpk_gt_i32 s12, 0x47f
	v_mov_b32_e32 v135, 0
	v_lshlrev_b32_e32 v136, 2, v2
	s_cbranch_scc1 .LBB0_366
	s_mul_hi_i32 s0, s12, 0x92492493
	s_add_i32 s0, s0, s12
	s_lshr_b32 s1, s0, 31
	s_ashr_i32 s0, s0, 11
	s_add_i32 s10, s0, s1
	s_mul_i32 s0, s10, 0xfffff200
	s_add_i32 s0, s0, s12
	s_mul_hi_i32 s1, s0, 0x92492493
	s_add_i32 s1, s1, s0
	s_lshr_b32 s2, s1, 31
	s_ashr_i32 s1, s1, 8
	s_add_i32 s8, s1, s2
	s_mul_i32 s1, s8, 0xfffffe40
	s_add_i32 s4, s1, s0
	s_mul_i32 s6, s8, 0x3800000
	s_mul_hi_i32 s5, s8, 0x3800000
	s_add_u32 s7, s52, s6
	s_addc_u32 s9, s53, s5
	s_lshl_b32 s0, s4, 4
	s_and_b32 s0, s0, 0xffffff80
	s_ashr_i32 s1, s0, 31
	s_lshl_b64 s[2:3], s[0:1], 13
	s_add_u32 s1, s7, s2
	s_addc_u32 s2, s9, s3
	s_lshl_b32 s3, s12, 8
	s_and_b32 s11, s3, 0x700
	s_lshl_b32 s7, s11, 2
	s_add_u32 s1, s1, s7
	s_addc_u32 s2, s2, 0
	s_mul_i32 s9, s8, 0xe00000
	s_mul_hi_i32 s7, s8, 0xe00000
	s_add_u32 s14, s88, s9
	s_addc_u32 s15, s89, s7
	s_mul_hi_i32 s7, s4, 0x92492493
	s_add_i32 s7, s7, s4
	s_lshr_b32 s9, s7, 31
	s_ashr_i32 s7, s7, 4
	s_add_i32 s7, s7, s9
	s_mul_i32 s9, s7, 0xffffffe4
	s_add_i32 s9, s9, s4
	s_add_i32 s4, s12, 0xdff
	v_readlane_b32 s16, v251, 0
	s_cmpk_lt_u32 s4, 0x1bff
	v_readlane_b32 s20, v251, 4
	v_readlane_b32 s22, v251, 6
	v_readlane_b32 s21, v251, 5
	v_readlane_b32 s23, v251, 7
	s_cselect_b32 s16, s20, s22
	s_cselect_b32 s4, s21, s23
	s_add_u32 s6, s16, s6
	v_readlane_b32 s17, v251, 1
	s_addc_u32 s4, s4, s5
	s_lshl_b32 s16, s7, 7
	s_mul_i32 s7, s7, 0x380000
	v_readlane_b32 s18, v251, 2
	s_mul_hi_i32 s5, s16, 0x7000
	s_add_u32 s17, s6, s7
	s_addc_u32 s18, s4, s5
	s_lshl_b32 s4, s9, 8
	s_ashr_i32 s5, s4, 31
	s_lshl_b64 s[6:7], s[4:5], 2
	s_add_u32 s5, s17, s6
	s_addc_u32 s6, s18, s7
	s_mul_hi_i32 s7, s8, 0x1c00000
	s_mul_i32 s8, s8, 0x1c00000
	s_add_u32 s17, s90, s8
	s_addc_u32 s7, s91, s7
	s_cmpk_lt_i32 s12, 0x1c00
	s_cselect_b32 s8, s5, s1
	s_movk_i32 s1, 0x800
	s_cselect_b32 s1, 0x1c00, s1
	v_mul_u32_u24_e32 v2, s1, v141
	s_cselect_b32 s9, s6, s2
	v_lshlrev_b32_e32 v134, 2, v2
	v_lshl_add_u64 v[2:3], s[8:9], 0, v[134:135]
	v_mov_b32_e32 v137, v135
	s_mov_b32 s3, 0
	s_cselect_b32 s10, s10, 2
	s_cselect_b32 s4, s4, s11
	s_cselect_b32 s0, s16, s0
	s_cselect_b32 s7, s7, s15
	s_cselect_b32 s6, s17, s14
	v_lshl_add_u64 v[2:3], v[2:3], 0, v[136:137]
	s_lshl_b32 s2, s1, 5
	s_waitcnt vmcnt(0)
	v_lshl_add_u64 v[10:11], v[2:3], 0, s[2:3]
	global_load_dwordx4 v[2:5], v[2:3], off nt
	s_waitcnt lgkmcnt(0)
	global_load_dwordx4 v[6:9], v[10:11], off nt
	v_lshl_add_u64 v[10:11], v[10:11], 0, s[2:3]
	v_lshl_add_u64 v[18:19], v[10:11], 0, s[2:3]
	global_load_dwordx4 v[10:13], v[10:11], off nt
	s_nop 0
	global_load_dwordx4 v[14:17], v[18:19], off nt
	v_lshl_add_u64 v[18:19], v[18:19], 0, s[2:3]
	v_lshl_add_u64 v[26:27], v[18:19], 0, s[2:3]
	global_load_dwordx4 v[18:21], v[18:19], off nt
	s_nop 0
	global_load_dwordx4 v[22:25], v[26:27], off nt
	v_lshl_add_u64 v[26:27], v[26:27], 0, s[2:3]
	v_lshl_add_u64 v[34:35], v[26:27], 0, s[2:3]
	v_lshl_add_u64 v[38:39], v[34:35], 0, s[2:3]
	v_lshl_add_u64 v[42:43], v[38:39], 0, s[2:3]
	v_lshl_add_u64 v[46:47], v[42:43], 0, s[2:3]
	v_lshl_add_u64 v[50:51], v[46:47], 0, s[2:3]
	v_lshl_add_u64 v[54:55], v[50:51], 0, s[2:3]
	v_lshl_add_u64 v[58:59], v[54:55], 0, s[2:3]
	v_lshl_add_u64 v[62:63], v[58:59], 0, s[2:3]
	global_load_dwordx4 v[26:29], v[26:27], off nt
	s_nop 0
	global_load_dwordx4 v[30:33], v[34:35], off nt
	v_readlane_b32 s19, v251, 3
	global_load_dwordx4 v[34:37], v[38:39], off nt
	s_nop 0
	global_load_dwordx4 v[38:41], v[42:43], off nt
	s_nop 0
	global_load_dwordx4 v[42:45], v[46:47], off nt
	s_nop 0
	global_load_dwordx4 v[46:49], v[50:51], off nt
	s_nop 0
	global_load_dwordx4 v[50:53], v[54:55], off nt
	s_nop 0
	global_load_dwordx4 v[54:57], v[58:59], off nt
	s_nop 0
	global_load_dwordx4 v[58:61], v[62:63], off nt
	v_lshl_add_u64 v[62:63], v[62:63], 0, s[2:3]
	global_load_dwordx4 v[62:65], v[62:63], off nt
	s_branch .LBB0_367

.LBB0_370:
	s_cmpk_gt_i32 s18, 0x47f
	s_mov_b64 s[42:43], -1
	s_cbranch_scc1 .LBB0_369
	s_add_i32 s18, s18, s13
	s_cmpk_lt_i32 s18, 0x480
	s_cselect_b64 s[44:45], -1, 0
	s_cmpk_gt_i32 s18, 0x47f
	s_cselect_b64 s[42:43], -1, 0
	s_and_b64 vcc, exec, s[42:43]
	s_cbranch_vccnz .LBB0_378
	s_mul_hi_i32 s1, s18, 0x92492493
	s_add_i32 s1, s1, s18
	s_lshr_b32 s2, s1, 31
	s_ashr_i32 s1, s1, 11
	s_add_i32 s17, s1, s2
	s_mul_i32 s1, s17, 0xfffff200
	s_add_i32 s2, s1, s18
	s_mul_hi_i32 s1, s2, 0x92492493
	s_add_i32 s1, s1, s2
	s_lshr_b32 s3, s1, 31
	s_ashr_i32 s1, s1, 8
	s_add_i32 s1, s1, s3
	s_mul_i32 s19, s1, 0xfffffe40
	s_add_i32 s19, s19, s2
	s_mov_b64 s[46:47], -1
	s_cmpk_gt_i32 s18, 0x1bff
	s_mul_hi_i32 s5, s1, 0x3800000
	s_mul_i32 s8, s1, 0x3800000
	s_cbranch_scc0 .LBB0_374
	s_add_u32 s20, s52, s8
	s_addc_u32 s21, s53, s5
	s_lshl_b32 s2, s19, 4
	s_and_b32 s14, s2, 0xffffff80
	s_ashr_i32 s15, s14, 31
	s_lshl_b64 s[2:3], s[14:15], 13
	s_add_u32 s2, s20, s2
	s_addc_u32 s3, s21, s3
	s_lshl_b32 s15, s18, 8
	s_and_b32 s36, s15, 0x700
	s_lshl_b32 s15, s36, 2
	s_add_u32 s2, s2, s15
	s_addc_u32 s3, s3, 0
	s_mul_i32 s20, s1, 0xe00000
	s_mul_hi_i32 s15, s1, 0xe00000
	s_add_u32 s40, s88, s20
	s_addc_u32 s41, s89, s15
	s_mov_b64 s[46:47], 0

.LBB0_394:
	s_andn2_b64 vcc, exec, s[44:45]
	s_waitcnt lgkmcnt(0)
	s_barrier
	s_cbranch_vccnz .LBB0_369
	s_add_i32 s18, s18, s13
	s_cmpk_gt_i32 s18, 0x47f
	s_cbranch_scc1 .LBB0_402
	s_mul_hi_i32 s0, s18, 0x92492493
	s_add_i32 s0, s0, s18
	s_lshr_b32 s1, s0, 31
	s_ashr_i32 s0, s0, 11
	s_add_i32 s10, s0, s1
	s_mul_i32 s0, s10, 0xfffff200
	s_add_i32 s0, s0, s18
	s_mul_hi_i32 s1, s0, 0x92492493
	s_add_i32 s1, s1, s0
	s_lshr_b32 s2, s1, 31
	s_ashr_i32 s8, s1, 8
	s_add_i32 s8, s8, s2
	s_mul_i32 s19, s8, 0xfffffe40
	s_add_i32 s19, s19, s0
	s_mov_b64 s[44:45], -1
	s_cmpk_gt_i32 s18, 0x1bff
	s_mul_hi_i32 s5, s8, 0x3800000
	s_mul_i32 s15, s8, 0x3800000
	s_cbranch_scc0 .LBB0_398
	s_add_u32 s4, s52, s15
	s_addc_u32 s6, s53, s5
	s_lshl_b32 s0, s19, 4
	s_and_b32 s0, s0, 0xffffff80
	s_ashr_i32 s1, s0, 31
	s_lshl_b64 s[2:3], s[0:1], 13
	s_add_u32 s1, s4, s2
	s_addc_u32 s3, s6, s3
	s_lshl_b32 s2, s18, 8
	s_and_b32 s4, s2, 0x700
	s_lshl_b32 s2, s4, 2
	s_add_u32 s2, s1, s2
	s_addc_u32 s3, s3, 0
	s_mul_i32 s6, s8, 0xe00000
	s_mul_hi_i32 s1, s8, 0xe00000
	s_add_u32 s6, s88, s6
	s_addc_u32 s7, s89, s1
	s_mov_b64 s[44:45], 0

.LBB0_839:
	s_add_u32 s16, s56, 0x3eb00000
	s_addc_u32 s17, s57, 0
	s_cmp_lt_i32 s58, 8
	s_cselect_b64 s[0:1], -1, 0
	s_cmp_gt_i32 s59, 7
	s_cselect_b64 s[2:3], -1, 0
	s_and_b64 s[0:1], s[0:1], s[2:3]
	s_andn2_b64 vcc, exec, s[0:1]
	s_cbranch_vccnz .LBB0_921
	s_mov_b32 s99, s13
	s_cmp_lt_u32 s12, 160
	s_cbranch_scc1 .Lsp7_gemm
	s_mov_b32 s98, s12
	s_add_i32 s12, s12, 992
	s_mov_b32 s13, 96
	v_lshrrev_b32_e32 v140, 3, v0
	s_add_u32 s0, s94, 0xffffffe0
	s_addc_u32 s1, s95, -1
	s_load_dwordx2 s[52:53], s[0:1], 0x0
	s_waitcnt lgkmcnt(0)
	s_branch .Lcv_364
.Lsp7_gemm:
	s_mov_b32 s13, 160
	s_cmpk_gt_i32 s12, 0xaff
	v_readfirstlane_b32 s3, v0
	s_cbranch_scc1 .LBB0_867
	v_lshlrev_b32_e32 v2, 4, v0
	v_and_b32_e32 v3, 32, v0
	v_bitop3_b32 v2, v2, v3, 48 bitop3:0x6c
	v_lshrrev_b32_e32 v3, 1, v0
	v_lshrrev_b32_e32 v5, 5, v0
	v_and_b32_e32 v3, 24, v3
	v_and_b32_e32 v5, 4, v5
	s_waitcnt vmcnt(14)
	v_bfe_u32 v6, v0, 2, 2
	v_bfe_u32 v4, v0, 2, 4
	v_or3_b32 v3, v5, v6, v3
	v_lshrrev_b32_e32 v5, 3, v0
	v_and_or_b32 v2, v0, 64, v2
	v_and_or_b32 v6, v5, 48, v4
	v_and_or_b32 v5, v5, 32, v3
	s_lshr_b32 s6, s3, 6
	v_lshl_or_b32 v202, v5, 11, v2
	v_bfe_u32 v5, v0, 3, 25
	s_lshr_b32 s14, s3, 8
	s_lshl_b32 s10, s6, 10
	v_or_b32_e32 v5, 64, v5
	s_movk_i32 s0, 0x70
	s_add_u32 s11, s56, 0x4db00000
	v_and_or_b32 v4, v5, s0, v4
	s_movk_i32 s0, 0x60
	s_addc_u32 s18, s57, 0
	s_ashr_i32 s19, s12, 31
	v_and_or_b32 v3, v5, s0, v3
	s_lshr_b32 s0, s19, 29
	s_add_i32 s0, s12, s0
	s_ashr_i32 s1, s0, 3
	s_and_b32 s0, s0, -8
	s_sub_i32 s0, s12, s0
	s_cmp_lt_i32 s0, 0
	s_movk_i32 s20, 0x161
	s_cselect_b32 s2, s20, 0x160
	s_mul_i32 s0, s0, s2
	s_add_i32 s0, s0, s1
	s_mul_hi_i32 s1, s0, 0x2e8ba2e9
	s_lshr_b32 s2, s1, 31
	s_ashr_i32 s1, s1, 6
	s_add_i32 s1, s1, s2
	s_lshl_b32 s4, s1, 3
	s_mulk_i32 s1, 0x160
	s_sub_i32 s0, s0, s1
	s_sext_i32_i16 s1, s0
	s_bfe_u32 s1, s1, 0x3001c
	s_add_i32 s1, s0, s1
	s_sext_i32_i16 s2, s1
	s_and_b32 s1, s1, 0xfff8
	s_sub_i32 s0, s0, s1
	s_sext_i32_i16 s0, s0
	s_add_i32 s0, s4, s0
	s_ashr_i32 s1, s0, 31
	s_lshr_b32 s2, s2, 3
	s_lshl_b64 s[4:5], s[0:1], 19
	s_add_u32 s26, s24, s4
	s_addc_u32 s27, s25, s5
	s_bfe_i64 s[4:5], s[2:3], 0x100000
	s_lshl_b64 s[4:5], s[4:5], 19
	s_add_u32 s8, s11, s4
	s_addc_u32 s9, s18, s5
	s_add_i32 s1, s10, 0
	v_lshl_or_b32 v201, v6, 11, v2
	v_lshl_or_b32 v203, v4, 11, v2
	v_lshl_or_b32 v204, v3, 11, v2
	s_mov_b64 s[4:5], s[8:9]
	s_add_i32 s21, s1, 0x10000
	v_mov_b32_e32 v2, v202
	s_mov_b32 m0, s21
	s_add_i32 s33, s1, 0x12000
	global_load_lds_dwordx4 v2, s[4:5]
	v_mov_b32_e32 v2, v204
	s_mov_b32 m0, s33
	s_mov_b32 s7, 0
	global_load_lds_dwordx4 v2, s[4:5]
	s_add_u32 s4, s8, 0x40000
	s_addc_u32 s5, s9, 0
	s_add_i32 s35, s1, 0x14000
	v_mov_b32_e32 v2, v202
	s_mov_b32 m0, s35
	s_add_i32 s60, s1, 0x16000
	global_load_lds_dwordx4 v2, s[4:5]
	v_mov_b32_e32 v2, v204
	s_mov_b32 m0, s60
	s_add_i32 s61, s1, 0x2000
	global_load_lds_dwordx4 v2, s[4:5]
	s_mov_b64 s[4:5], s[26:27]
	v_mov_b32_e32 v2, v201
	s_mov_b32 m0, s1
	s_nop 0
	global_load_lds_dwordx4 v2, s[4:5]
	v_mov_b32_e32 v2, v203
	s_mov_b32 m0, s61
	s_nop 0
	global_load_lds_dwordx4 v2, s[4:5]
	s_add_u32 s4, s26, 0x40000
	s_addc_u32 s5, s27, 0
	s_add_i32 s62, s1, 0x4000
	v_mov_b32_e32 v2, v201
	s_mov_b32 m0, s62
	s_add_i32 s63, s1, 0x6000
	global_load_lds_dwordx4 v2, s[4:5]
	v_mov_b32_e32 v2, v203
	s_mov_b32 m0, s63
	s_cmp_eq_u32 s14, 1
	global_load_lds_dwordx4 v2, s[4:5]
	s_cselect_b64 s[4:5], -1, 0
	s_cmp_lg_u32 s14, 1
	s_cbranch_scc1 .LBB0_843
	s_barrier

.Lcv_364:
	v_and_b32_e32 v2, 0xfc, v200
	v_lshrrev_b32_e32 v141, 6, v0
	s_cmpk_gt_i32 s12, 0x29ff
	v_mov_b32_e32 v135, 0
	v_lshlrev_b32_e32 v136, 2, v2
	s_cbranch_scc1 .Lcv_366
	s_mul_hi_i32 s0, s12, 0x92492493
	s_add_i32 s0, s0, s12
	s_lshr_b32 s1, s0, 31
	s_ashr_i32 s0, s0, 11
	s_add_i32 s10, s0, s1
	s_mul_i32 s0, s10, 0xfffff200
	s_add_i32 s0, s0, s12
	s_mul_hi_i32 s1, s0, 0x92492493
	s_add_i32 s1, s1, s0
	s_lshr_b32 s2, s1, 31
	s_ashr_i32 s1, s1, 8
	s_add_i32 s8, s1, s2
	s_mul_i32 s1, s8, 0xfffffe40
	s_add_i32 s4, s1, s0
	s_mul_i32 s6, s8, 0x3800000
	s_mul_hi_i32 s5, s8, 0x3800000
	s_add_u32 s7, s52, s6
	s_addc_u32 s9, s53, s5
	s_lshl_b32 s0, s4, 4
	s_and_b32 s0, s0, 0xffffff80
	s_ashr_i32 s1, s0, 31
	s_lshl_b64 s[2:3], s[0:1], 13
	s_add_u32 s1, s7, s2
	s_addc_u32 s2, s9, s3
	s_lshl_b32 s3, s12, 8
	s_and_b32 s11, s3, 0x700
	s_lshl_b32 s7, s11, 2
	s_add_u32 s1, s1, s7
	s_addc_u32 s2, s2, 0
	s_mul_i32 s9, s8, 0xe00000
	s_mul_hi_i32 s7, s8, 0xe00000
	s_add_u32 s14, s88, s9
	s_addc_u32 s15, s89, s7
	s_mul_hi_i32 s7, s4, 0x92492493
	s_add_i32 s7, s7, s4
	s_lshr_b32 s9, s7, 31
	s_ashr_i32 s7, s7, 4
	s_add_i32 s7, s7, s9
	s_mul_i32 s9, s7, 0xffffffe4
	s_add_i32 s9, s9, s4
	s_add_i32 s4, s12, 0xdff
	v_readlane_b32 s68, v251, 0
	s_cmpk_lt_u32 s4, 0x1bff
	v_readlane_b32 s20, v251, 4
	v_readlane_b32 s70, v251, 6
	v_readlane_b32 s21, v251, 5
	v_readlane_b32 s71, v251, 7
	s_cselect_b32 s68, s20, s70
	s_cselect_b32 s4, s21, s71
	s_add_u32 s6, s68, s6
	v_readlane_b32 s69, v251, 1
	s_addc_u32 s4, s4, s5
	s_lshl_b32 s68, s7, 7
	s_mul_i32 s7, s7, 0x380000
	v_readlane_b32 s18, v251, 2
	s_mul_hi_i32 s5, s68, 0x7000
	s_add_u32 s69, s6, s7
	s_addc_u32 s18, s4, s5
	s_lshl_b32 s4, s9, 8
	s_ashr_i32 s5, s4, 31
	s_lshl_b64 s[6:7], s[4:5], 2
	s_add_u32 s5, s69, s6
	s_addc_u32 s6, s18, s7
	s_mul_hi_i32 s7, s8, 0x1c00000
	s_mul_i32 s8, s8, 0x1c00000
	s_add_u32 s69, s90, s8
	s_addc_u32 s7, s91, s7
	s_cmpk_lt_i32 s12, 0x1c00
	s_cselect_b32 s8, s5, s1
	s_movk_i32 s1, 0x800
	s_cselect_b32 s1, 0x1c00, s1
	v_mul_u32_u24_e32 v2, s1, v141
	s_cselect_b32 s9, s6, s2
	v_lshlrev_b32_e32 v134, 2, v2
	v_lshl_add_u64 v[2:3], s[8:9], 0, v[134:135]
	v_mov_b32_e32 v137, v135
	s_mov_b32 s3, 0
	s_cselect_b32 s10, s10, 2
	s_cselect_b32 s4, s4, s11
	s_cselect_b32 s0, s68, s0
	s_cselect_b32 s7, s7, s15
	s_cselect_b32 s6, s69, s14
	v_lshl_add_u64 v[2:3], v[2:3], 0, v[136:137]
	s_lshl_b32 s2, s1, 5
	s_waitcnt vmcnt(0)
	v_lshl_add_u64 v[10:11], v[2:3], 0, s[2:3]
	global_load_dwordx4 v[2:5], v[2:3], off nt
	s_waitcnt lgkmcnt(0)
	global_load_dwordx4 v[6:9], v[10:11], off nt
	v_lshl_add_u64 v[10:11], v[10:11], 0, s[2:3]
	v_lshl_add_u64 v[18:19], v[10:11], 0, s[2:3]
	global_load_dwordx4 v[10:13], v[10:11], off nt
	s_nop 0
	global_load_dwordx4 v[14:17], v[18:19], off nt
	v_lshl_add_u64 v[18:19], v[18:19], 0, s[2:3]
	v_lshl_add_u64 v[26:27], v[18:19], 0, s[2:3]
	global_load_dwordx4 v[18:21], v[18:19], off nt
	s_nop 0
	global_load_dwordx4 v[22:25], v[26:27], off nt
	v_lshl_add_u64 v[26:27], v[26:27], 0, s[2:3]
	v_lshl_add_u64 v[34:35], v[26:27], 0, s[2:3]
	v_lshl_add_u64 v[38:39], v[34:35], 0, s[2:3]
	v_lshl_add_u64 v[42:43], v[38:39], 0, s[2:3]
	v_lshl_add_u64 v[46:47], v[42:43], 0, s[2:3]
	v_lshl_add_u64 v[50:51], v[46:47], 0, s[2:3]
	v_lshl_add_u64 v[54:55], v[50:51], 0, s[2:3]
	v_lshl_add_u64 v[58:59], v[54:55], 0, s[2:3]
	v_lshl_add_u64 v[62:63], v[58:59], 0, s[2:3]
	global_load_dwordx4 v[26:29], v[26:27], off nt
	s_nop 0
	global_load_dwordx4 v[30:33], v[34:35], off nt
	v_readlane_b32 s19, v251, 3
	global_load_dwordx4 v[34:37], v[38:39], off nt
	s_nop 0
	global_load_dwordx4 v[38:41], v[42:43], off nt
	s_nop 0
	global_load_dwordx4 v[42:45], v[46:47], off nt
	s_nop 0
	global_load_dwordx4 v[46:49], v[50:51], off nt
	s_nop 0
	global_load_dwordx4 v[50:53], v[54:55], off nt
	s_nop 0
	global_load_dwordx4 v[54:57], v[58:59], off nt
	s_nop 0
	global_load_dwordx4 v[58:61], v[62:63], off nt
	v_lshl_add_u64 v[62:63], v[62:63], 0, s[2:3]
	global_load_dwordx4 v[62:65], v[62:63], off nt
	s_branch .Lcv_367
.Lcv_366:
.Lcv_367:
	v_and_b32_e32 v66, 0x700, v200
	v_lshlrev_b32_e32 v66, 2, v66
	v_add3_u32 v142, 0, v66, v136
	v_and_b32_e32 v66, 0xff, v0
	v_lshrrev_b32_e32 v67, 8, v0
	v_or_b32_e32 v73, 0x200, v0
	v_or_b32_e32 v76, 0x600, v0
	v_lshlrev_b32_e32 v68, 16, v67
	v_lshlrev_b32_e32 v69, 2, v66
	v_lshrrev_b32_e32 v152, 3, v73
	v_lshrrev_b32_e32 v154, 3, v76
	v_add3_u32 v151, 0, v68, v69
	v_lshlrev_b32_e32 v67, 2, v67
	v_and_b32_e32 v68, 7, v0
	v_xor_b32_e32 v72, v140, v0
	v_xor_b32_e32 v74, v152, v0
	v_xor_b32_e32 v77, v154, v0
	v_bitop3_b32 v69, v67, v0, 7 bitop3:0x78
	v_bitop3_b32 v70, v67, v68, 1 bitop3:0x36
	v_bitop3_b32 v71, v67, v68, 2 bitop3:0x36
	v_bitop3_b32 v67, v67, v68, 3 bitop3:0x36
	v_lshlrev_b32_e32 v72, 4, v72
	v_lshlrev_b32_e32 v74, 4, v74
	v_or_b32_e32 v153, 0x80, v140
	v_lshlrev_b32_e32 v77, 4, v77
	v_lshl_add_u32 v66, v66, 7, 0
	v_lshlrev_b32_e32 v69, 4, v69
	v_lshlrev_b32_e32 v70, 4, v70
	v_lshlrev_b32_e32 v71, 4, v71
	v_lshlrev_b32_e32 v67, 4, v67
	v_lshlrev_b32_e32 v138, 4, v68
	v_lshl_add_u32 v68, v140, 7, 0
	v_and_b32_e32 v72, 0x70, v72
	v_lshl_add_u32 v73, v152, 7, 0
	v_and_b32_e32 v74, 0x70, v74
	v_lshl_add_u32 v75, v153, 7, 0
	v_lshl_add_u32 v76, v154, 7, 0
	v_and_b32_e32 v77, 0x70, v77
	s_mov_b32 s9, 0
	v_add_u32_e32 v143, 0x10000, v142
	v_add_u32_e32 v144, 0x12000, v142
	v_add_u32_e32 v145, 0x14000, v142
	v_add_u32_e32 v146, 0x16000, v142
	v_add_u32_e32 v147, 0x18000, v142
	v_add_u32_e32 v148, 0x1a000, v142
	v_add_u32_e32 v149, 0x1c000, v142
	v_add_u32_e32 v150, 0x1e000, v142
	v_mov_b32_e32 v139, v135
	s_mov_b32 s11, 0xc3e00000
	s_movk_i32 s68, 0x3c0
	v_mov_b32_e32 v155, 0x43e00000
	v_add_u32_e32 v156, v66, v69
	v_add_u32_e32 v157, v66, v70
	v_add_u32_e32 v158, v66, v71
	v_add_u32_e32 v159, v66, v67
	v_add_u32_e32 v160, v68, v72
	v_add_u32_e32 v161, v73, v74
	v_add_u32_e32 v162, v75, v72
	v_add_u32_e32 v163, v76, v77
	s_mov_b32 s18, s12
	s_branch .Lcv_370

.Lcv_370:
	s_cmpk_gt_i32 s18, 0x29ff
	s_mov_b64 s[42:43], -1
	s_cbranch_scc1 .Lcv_369
	s_add_i32 s18, s18, s13
	s_cmpk_lt_i32 s18, 0x2a00
	s_cselect_b64 s[44:45], -1, 0
	s_cmpk_gt_i32 s18, 0x29ff
	s_cselect_b64 s[42:43], -1, 0
	s_and_b64 vcc, exec, s[42:43]
	s_cbranch_vccnz .Lcv_378
	s_mul_hi_i32 s1, s18, 0x92492493
	s_add_i32 s1, s1, s18
	s_lshr_b32 s2, s1, 31
	s_ashr_i32 s1, s1, 11
	s_add_i32 s69, s1, s2
	s_mul_i32 s1, s69, 0xfffff200
	s_add_i32 s2, s1, s18
	s_mul_hi_i32 s1, s2, 0x92492493
	s_add_i32 s1, s1, s2
	s_lshr_b32 s3, s1, 31
	s_ashr_i32 s1, s1, 8
	s_add_i32 s1, s1, s3
	s_mul_i32 s19, s1, 0xfffffe40
	s_add_i32 s19, s19, s2
	s_mov_b64 s[46:47], -1
	s_cmpk_gt_i32 s18, 0x1bff
	s_mul_hi_i32 s5, s1, 0x3800000
	s_mul_i32 s8, s1, 0x3800000
	s_cbranch_scc0 .Lcv_374
	s_add_u32 s20, s52, s8
	s_addc_u32 s21, s53, s5
	s_lshl_b32 s2, s19, 4
	s_and_b32 s14, s2, 0xffffff80
	s_ashr_i32 s15, s14, 31
	s_lshl_b64 s[2:3], s[14:15], 13
	s_add_u32 s2, s20, s2
	s_addc_u32 s3, s21, s3
	s_lshl_b32 s15, s18, 8
	s_and_b32 s72, s15, 0x700
	s_lshl_b32 s15, s72, 2
	s_add_u32 s2, s2, s15
	s_addc_u32 s3, s3, 0
	s_mul_i32 s20, s1, 0xe00000
	s_mul_hi_i32 s15, s1, 0xe00000
	s_add_u32 s40, s88, s20
	s_addc_u32 s41, s89, s15
	s_mov_b64 s[46:47], 0
.Lcv_374:
	s_andn2_b64 vcc, exec, s[46:47]
	s_cbranch_vccnz .Lcv_376
	s_mul_hi_i32 s2, s19, 0x92492493
	s_add_i32 s2, s2, s19
	s_lshr_b32 s3, s2, 31
	s_ashr_i32 s2, s2, 4
	s_add_i32 s2, s2, s3
	s_mul_i32 s3, s2, 0xffffffe4
	s_add_i32 s3, s3, s19
	s_add_i32 s14, s18, 0xdff
	v_readlane_b32 s60, v251, 0
	s_cmpk_lt_u32 s14, 0x1bff
	v_readlane_b32 s64, v251, 4
	v_readlane_b32 s66, v251, 6
	v_readlane_b32 s65, v251, 5
	v_readlane_b32 s67, v251, 7
	s_cselect_b32 s15, s64, s66
	s_cselect_b32 s14, s65, s67
	s_add_u32 s8, s15, s8
	s_addc_u32 s5, s14, s5
	s_lshl_b32 s14, s2, 7
	s_mul_i32 s2, s2, 0x380000
	s_mul_hi_i32 s15, s14, 0x7000
	s_add_u32 s8, s8, s2
	s_addc_u32 s5, s5, s15
	s_lshl_b32 s72, s3, 8
	s_ashr_i32 s73, s72, 31
	s_lshl_b64 s[2:3], s[72:73], 2
	s_add_u32 s2, s8, s2
	s_addc_u32 s3, s5, s3
	s_mul_hi_i32 s5, s1, 0x1c00000
	s_mul_i32 s1, s1, 0x1c00000
	s_add_u32 s40, s90, s1
	s_addc_u32 s41, s91, s5
	s_mov_b64 s[46:47], 0x1c00
	v_readlane_b32 s61, v251, 1
	v_readlane_b32 s62, v251, 2
	v_readlane_b32 s63, v251, 3
	s_branch .Lcv_377
.Lcv_376:
	s_mov_b32 s69, 2
	s_mov_b64 s[46:47], 0x800

.Lcv_378:
	s_waitcnt vmcnt(0)
	ds_write_b128 v142, v[2:5]
	s_waitcnt lgkmcnt(1)
	ds_write_b128 v142, v[6:9] offset:8192
	ds_write_b128 v142, v[10:13] offset:16384
	ds_write_b128 v142, v[14:17] offset:24576
	ds_write_b128 v142, v[18:21] offset:32768
	ds_write_b128 v142, v[22:25] offset:40960
	ds_write_b128 v142, v[26:29] offset:49152
	ds_write_b128 v142, v[30:33] offset:57344
	ds_write_b128 v143, v[34:37]
	ds_write_b128 v144, v[38:41]
	ds_write_b128 v145, v[42:45]
	ds_write_b128 v146, v[46:49]
	ds_write_b128 v147, v[50:53]
	ds_write_b128 v148, v[54:57]
	ds_write_b128 v149, v[58:61]
	ds_write_b128 v150, v[62:65]
	s_waitcnt lgkmcnt(0)
	s_barrier
	ds_read2st64_b32 v[130:131], v151 offset1:4
	ds_read2st64_b32 v[132:133], v151 offset0:8 offset1:12
	ds_read2st64_b32 v[164:165], v151 offset0:24 offset1:28
	ds_read2st64_b32 v[166:167], v151 offset0:56 offset1:60
	s_cmp_gt_i32 s10, 1
	s_waitcnt lgkmcnt(3)
	v_mul_f32_e32 v130, 0x43000000, v130
	v_mul_f32_e32 v131, 0x43000000, v131
	s_waitcnt lgkmcnt(2)
	v_mul_f32_e32 v134, 0x43000000, v132
	v_med3_f32 v132, v130, s11, v155
	v_med3_f32 v131, v131, s11, v155
	v_mov_b32_e32 v130, v135
	v_mul_f32_e32 v137, 0x43000000, v133
	v_cvt_pk_fp8_f32 v130, v132, v131
	ds_read2st64_b32 v[132:133], v151 offset0:16 offset1:20
	v_med3_f32 v131, v134, s11, v155
	v_med3_f32 v134, v137, s11, v155
	v_cvt_pk_fp8_f32 v130, v131, v134 op_sel:[0,0,1]
	s_waitcnt lgkmcnt(2)
	v_mul_f32_e32 v134, 0x43000000, v164
	s_waitcnt lgkmcnt(0)
	v_mul_f32_e32 v131, 0x43000000, v132
	v_mul_f32_e32 v132, 0x43000000, v133
	v_med3_f32 v133, v131, s11, v155
	v_med3_f32 v132, v132, s11, v155
	v_mov_b32_e32 v131, v135
	v_cvt_pk_fp8_f32 v131, v133, v132
	ds_read2st64_b32 v[132:133], v151 offset0:32 offset1:36
	v_mul_f32_e32 v137, 0x43000000, v165
	ds_read2st64_b32 v[164:165], v151 offset0:40 offset1:44
	v_med3_f32 v134, v134, s11, v155
	v_med3_f32 v137, v137, s11, v155
	s_waitcnt lgkmcnt(1)
	v_mul_f32_e32 v132, 0x43000000, v132
	v_mul_f32_e32 v133, 0x43000000, v133
	v_cvt_pk_fp8_f32 v131, v134, v137 op_sel:[0,0,1]
	s_waitcnt lgkmcnt(0)
	v_mul_f32_e32 v134, 0x43000000, v164
	v_med3_f32 v164, v132, s11, v155
	v_med3_f32 v133, v133, s11, v155
	v_mov_b32_e32 v132, v135
	v_mul_f32_e32 v137, 0x43000000, v165
	v_cvt_pk_fp8_f32 v132, v164, v133
	ds_read2st64_b32 v[164:165], v151 offset0:48 offset1:52
	v_med3_f32 v133, v134, s11, v155
	v_med3_f32 v134, v137, s11, v155
	v_cvt_pk_fp8_f32 v132, v133, v134 op_sel:[0,0,1]
	v_mul_f32_e32 v137, 0x43000000, v166
	s_waitcnt lgkmcnt(0)
	v_mul_f32_e32 v133, 0x43000000, v164
	v_mul_f32_e32 v134, 0x43000000, v165
	v_med3_f32 v164, v133, s11, v155
	v_med3_f32 v134, v134, s11, v155
	v_mov_b32_e32 v133, v135
	v_cvt_pk_fp8_f32 v133, v164, v134
	ds_read2st64_b32 v[164:165], v151 offset0:64 offset1:68
	v_mul_f32_e32 v168, 0x43000000, v167
	ds_read2st64_b32 v[166:167], v151 offset0:72 offset1:76
	v_med3_f32 v134, v137, s11, v155
	v_med3_f32 v137, v168, s11, v155
	v_cvt_pk_fp8_f32 v133, v134, v137 op_sel:[0,0,1]
	s_waitcnt lgkmcnt(1)
	v_mul_f32_e32 v134, 0x43000000, v164
	v_mul_f32_e32 v137, 0x43000000, v165
	s_waitcnt lgkmcnt(0)
	v_mul_f32_e32 v165, 0x43000000, v166
	v_mul_f32_e32 v170, 0x43000000, v167
	v_med3_f32 v134, v134, s11, v155
	v_med3_f32 v137, v137, s11, v155
	v_mov_b32_e32 v164, v135
	ds_read2st64_b32 v[166:167], v151 offset0:80 offset1:84
	v_cvt_pk_fp8_f32 v164, v134, v137
	ds_read2st64_b32 v[168:169], v151 offset0:88 offset1:92
	v_med3_f32 v134, v165, s11, v155
	v_med3_f32 v137, v170, s11, v155
	v_cvt_pk_fp8_f32 v164, v134, v137 op_sel:[0,0,1]
	s_waitcnt lgkmcnt(1)
	v_mul_f32_e32 v134, 0x43000000, v166
	v_mul_f32_e32 v137, 0x43000000, v167
	s_waitcnt lgkmcnt(0)
	v_mul_f32_e32 v168, 0x43000000, v168
	v_med3_f32 v134, v134, s11, v155
	v_med3_f32 v137, v137, s11, v155
	v_mov_b32_e32 v165, v135
	ds_read2st64_b32 v[166:167], v151 offset0:96 offset1:100
	v_mul_f32_e32 v170, 0x43000000, v169
	v_cvt_pk_fp8_f32 v165, v134, v137
	v_med3_f32 v134, v168, s11, v155
	ds_read2st64_b32 v[168:169], v151 offset0:104 offset1:108
	v_med3_f32 v137, v170, s11, v155
	v_cvt_pk_fp8_f32 v165, v134, v137 op_sel:[0,0,1]
	s_waitcnt lgkmcnt(1)
	v_mul_f32_e32 v134, 0x43000000, v166
	v_mul_f32_e32 v137, 0x43000000, v167
	s_waitcnt lgkmcnt(0)
	v_mul_f32_e32 v167, 0x43000000, v168
	v_mul_f32_e32 v172, 0x43000000, v169
	v_med3_f32 v134, v134, s11, v155
	v_med3_f32 v137, v137, s11, v155
	v_mov_b32_e32 v166, v135
	ds_read2st64_b32 v[168:169], v151 offset0:112 offset1:116
	v_cvt_pk_fp8_f32 v166, v134, v137
	ds_read2st64_b32 v[170:171], v151 offset0:120 offset1:124
	v_med3_f32 v134, v167, s11, v155
	v_med3_f32 v137, v172, s11, v155
	v_cvt_pk_fp8_f32 v166, v134, v137 op_sel:[0,0,1]
	s_waitcnt lgkmcnt(1)
	v_mul_f32_e32 v134, 0x43000000, v168
	v_mul_f32_e32 v137, 0x43000000, v169
	s_waitcnt lgkmcnt(0)
	v_mul_f32_e32 v170, 0x43000000, v170
	v_med3_f32 v134, v134, s11, v155
	v_med3_f32 v137, v137, s11, v155
	v_mov_b32_e32 v167, v135
	ds_read2st64_b32 v[168:169], v151 offset0:128 offset1:132
	v_mul_f32_e32 v172, 0x43000000, v171
	v_cvt_pk_fp8_f32 v167, v134, v137
	v_med3_f32 v134, v170, s11, v155
	ds_read2st64_b32 v[170:171], v151 offset0:136 offset1:140
	v_med3_f32 v137, v172, s11, v155
	v_cvt_pk_fp8_f32 v167, v134, v137 op_sel:[0,0,1]
	s_waitcnt lgkmcnt(1)
	v_mul_f32_e32 v134, 0x43000000, v168
	v_mul_f32_e32 v137, 0x43000000, v169
	s_waitcnt lgkmcnt(0)
	v_mul_f32_e32 v169, 0x43000000, v170
	v_mul_f32_e32 v174, 0x43000000, v171
	v_med3_f32 v134, v134, s11, v155
	v_med3_f32 v137, v137, s11, v155
	v_mov_b32_e32 v168, v135
	ds_read2st64_b32 v[170:171], v151 offset0:144 offset1:148
	v_cvt_pk_fp8_f32 v168, v134, v137
	ds_read2st64_b32 v[172:173], v151 offset0:152 offset1:156
	v_med3_f32 v134, v169, s11, v155
	v_med3_f32 v137, v174, s11, v155
	v_cvt_pk_fp8_f32 v168, v134, v137 op_sel:[0,0,1]
	s_waitcnt lgkmcnt(1)
	v_mul_f32_e32 v134, 0x43000000, v170
	v_mul_f32_e32 v137, 0x43000000, v171
	s_waitcnt lgkmcnt(0)
	v_mul_f32_e32 v172, 0x43000000, v172
	v_med3_f32 v134, v134, s11, v155
	v_med3_f32 v137, v137, s11, v155
	v_mov_b32_e32 v169, v135
	ds_read2st64_b32 v[170:171], v151 offset0:160 offset1:164
	v_mul_f32_e32 v174, 0x43000000, v173
	v_cvt_pk_fp8_f32 v169, v134, v137
	v_med3_f32 v134, v172, s11, v155
	ds_read2st64_b32 v[172:173], v151 offset0:168 offset1:172
	v_med3_f32 v137, v174, s11, v155
	v_cvt_pk_fp8_f32 v169, v134, v137 op_sel:[0,0,1]
	s_waitcnt lgkmcnt(1)
	v_mul_f32_e32 v134, 0x43000000, v170
	v_mul_f32_e32 v137, 0x43000000, v171
	s_waitcnt lgkmcnt(0)
	v_mul_f32_e32 v171, 0x43000000, v172
	v_mul_f32_e32 v176, 0x43000000, v173
	v_med3_f32 v134, v134, s11, v155
	v_med3_f32 v137, v137, s11, v155
	v_mov_b32_e32 v170, v135
	ds_read2st64_b32 v[172:173], v151 offset0:176 offset1:180
	v_cvt_pk_fp8_f32 v170, v134, v137
	ds_read2st64_b32 v[174:175], v151 offset0:184 offset1:188
	v_med3_f32 v134, v171, s11, v155
	v_med3_f32 v137, v176, s11, v155
	v_cvt_pk_fp8_f32 v170, v134, v137 op_sel:[0,0,1]
	s_waitcnt lgkmcnt(1)
	v_mul_f32_e32 v134, 0x43000000, v172
	v_mul_f32_e32 v137, 0x43000000, v173
	s_waitcnt lgkmcnt(0)
	v_mul_f32_e32 v174, 0x43000000, v174
	v_med3_f32 v134, v134, s11, v155
	v_med3_f32 v137, v137, s11, v155
	v_mov_b32_e32 v171, v135
	ds_read2st64_b32 v[172:173], v151 offset0:192 offset1:196
	v_mul_f32_e32 v176, 0x43000000, v175
	v_cvt_pk_fp8_f32 v171, v134, v137
	v_med3_f32 v134, v174, s11, v155
	ds_read2st64_b32 v[174:175], v151 offset0:200 offset1:204
	v_med3_f32 v137, v176, s11, v155
	v_cvt_pk_fp8_f32 v171, v134, v137 op_sel:[0,0,1]
	s_waitcnt lgkmcnt(1)
	v_mul_f32_e32 v134, 0x43000000, v172
	v_mul_f32_e32 v137, 0x43000000, v173
	s_waitcnt lgkmcnt(0)
	v_mul_f32_e32 v173, 0x43000000, v174
	v_mul_f32_e32 v178, 0x43000000, v175
	v_med3_f32 v134, v134, s11, v155
	v_med3_f32 v137, v137, s11, v155
	v_mov_b32_e32 v172, v135
	ds_read2st64_b32 v[174:175], v151 offset0:208 offset1:212
	v_cvt_pk_fp8_f32 v172, v134, v137
	ds_read2st64_b32 v[176:177], v151 offset0:216 offset1:220
	v_med3_f32 v134, v173, s11, v155
	v_med3_f32 v137, v178, s11, v155
	v_cvt_pk_fp8_f32 v172, v134, v137 op_sel:[0,0,1]
	s_waitcnt lgkmcnt(1)
	v_mul_f32_e32 v134, 0x43000000, v174
	v_mul_f32_e32 v137, 0x43000000, v175
	s_waitcnt lgkmcnt(0)
	v_mul_f32_e32 v176, 0x43000000, v176
	v_med3_f32 v134, v134, s11, v155
	v_med3_f32 v137, v137, s11, v155
	v_mov_b32_e32 v173, v135
	ds_read2st64_b32 v[174:175], v151 offset0:224 offset1:228
	v_mul_f32_e32 v178, 0x43000000, v177
	v_cvt_pk_fp8_f32 v173, v134, v137
	v_med3_f32 v134, v176, s11, v155
	ds_read2st64_b32 v[176:177], v151 offset0:232 offset1:236
	v_med3_f32 v137, v178, s11, v155
	v_cvt_pk_fp8_f32 v173, v134, v137 op_sel:[0,0,1]
	s_waitcnt lgkmcnt(1)
	v_mul_f32_e32 v134, 0x43000000, v174
	v_mul_f32_e32 v137, 0x43000000, v175
	s_waitcnt lgkmcnt(0)
	v_mul_f32_e32 v175, 0x43000000, v176
	v_mul_f32_e32 v180, 0x43000000, v177
	v_med3_f32 v134, v134, s11, v155
	v_med3_f32 v137, v137, s11, v155
	v_mov_b32_e32 v174, v135
	ds_read2st64_b32 v[176:177], v151 offset0:240 offset1:244
	v_cvt_pk_fp8_f32 v174, v134, v137
	v_med3_f32 v134, v175, s11, v155
	ds_read2st64_b32 v[178:179], v151 offset0:248 offset1:252
	v_med3_f32 v137, v180, s11, v155
	v_cvt_pk_fp8_f32 v174, v134, v137 op_sel:[0,0,1]
	s_waitcnt lgkmcnt(1)
	v_mul_f32_e32 v134, 0x43000000, v176
	v_mul_f32_e32 v137, 0x43000000, v177
	v_med3_f32 v134, v134, s11, v155
	v_med3_f32 v137, v137, s11, v155
	v_mov_b32_e32 v175, v135
	v_cvt_pk_fp8_f32 v175, v134, v137
	s_waitcnt lgkmcnt(0)
	v_mul_f32_e32 v176, 0x43000000, v178
	v_mul_f32_e32 v134, 0x43000000, v179
	v_med3_f32 v137, v176, s11, v155
	v_med3_f32 v134, v134, s11, v155
	v_cvt_pk_fp8_f32 v175, v137, v134 op_sel:[0,0,1]
	s_barrier
	ds_write_b128 v156, v[130:133]
	ds_write_b128 v157, v[164:167]
	ds_write_b128 v158, v[168:171]
	ds_write_b128 v159, v[172:175]
	s_waitcnt lgkmcnt(0)
	s_barrier
	ds_read_b128 v[130:133], v160
	v_add_u32_e32 v164, s4, v140
	s_cselect_b64 s[46:47], -1, 0
	s_mov_b64 s[2:3], -1
	s_and_b64 vcc, exec, s[46:47]
	v_lshlrev_b32_e32 v165, 1, v164
	v_add_u32_e32 v137, s0, v138
	s_cbranch_vccz .Lcv_380
	v_lshlrev_b32_e32 v134, 2, v164
	v_lshrrev_b32_e32 v166, 1, v164
	v_and_b32_e32 v167, 0xffffffe3, v164
	v_and_or_b32 v168, v166, 12, v167
	v_and_or_b32 v169, v134, 16, v167
	v_ashrrev_i32_e32 v166, 7, v164
	v_ashrrev_i32_e32 v134, 7, v137
	v_mad_u64_u32 v[166:167], s[2:3], v166, 56, v[134:135]
	v_lshrrev_b32_e32 v134, 3, v169
	v_bfe_u32 v169, v137, 6, 1
	v_ashrrev_i32_e32 v167, 31, v166
	v_and_or_b32 v134, v134, 14, v169
	v_lshlrev_b32_e32 v168, 6, v168
	v_and_b32_e32 v169, 63, v137
	v_lshlrev_b64 v[166:167], 14, v[166:167]
	v_and_or_b32 v168, v168, s68, v169
	v_lshlrev_b32_e32 v134, 10, v134
	v_and_b32_e32 v169, 32, v165
	v_bitop3_b32 v134, v134, v168, v169 bitop3:0xf6
	v_lshl_add_u64 v[166:167], s[6:7], 0, v[166:167]
	v_lshl_add_u64 v[166:167], v[166:167], 0, v[134:135]
	s_waitcnt lgkmcnt(0)
	global_store_dwordx4 v[166:167], v[130:133], off nt
	s_mov_b64 s[2:3], 0

.Lcv_382:
	s_waitcnt lgkmcnt(0)
	ds_read_b128 v[130:133], v161
	v_add_u32_e32 v164, s4, v152
	v_cndmask_b32_e64 v134, 0, 1, s[46:47]
	s_mov_b64 s[48:49], -1
	v_cmp_ne_u32_e64 s[2:3], 1, v134
	s_andn2_b64 vcc, exec, s[46:47]
	v_lshlrev_b32_e32 v165, 1, v164
	s_cbranch_vccnz .Lcv_384
	v_lshlrev_b32_e32 v134, 2, v164
	v_lshrrev_b32_e32 v166, 1, v164
	v_and_b32_e32 v167, 0xffffffe3, v164
	v_and_or_b32 v168, v166, 12, v167
	v_and_or_b32 v169, v134, 16, v167
	v_ashrrev_i32_e32 v166, 7, v164
	v_ashrrev_i32_e32 v134, 7, v137
	v_mad_u64_u32 v[166:167], s[20:21], v166, 56, v[134:135]
	v_lshrrev_b32_e32 v134, 3, v169
	v_bfe_u32 v169, v137, 6, 1
	v_ashrrev_i32_e32 v167, 31, v166
	v_and_or_b32 v134, v134, 14, v169
	v_lshlrev_b32_e32 v168, 6, v168
	v_and_b32_e32 v169, 63, v137
	v_lshlrev_b64 v[166:167], 14, v[166:167]
	v_and_or_b32 v168, v168, s68, v169
	v_lshlrev_b32_e32 v134, 10, v134
	v_and_b32_e32 v169, 32, v165
	v_bitop3_b32 v134, v134, v168, v169 bitop3:0xf6
	v_lshl_add_u64 v[166:167], s[6:7], 0, v[166:167]
	v_lshl_add_u64 v[166:167], v[166:167], 0, v[134:135]
	s_mov_b64 s[48:49], 0
	s_waitcnt lgkmcnt(0)
	global_store_dwordx4 v[166:167], v[130:133], off nt

.Lcv_386:
	s_waitcnt lgkmcnt(0)
	ds_read_b128 v[130:133], v162
	v_add_u32_e32 v164, s4, v153
	s_mov_b64 s[46:47], -1
	s_and_b64 vcc, exec, s[2:3]
	v_lshlrev_b32_e32 v165, 1, v164
	s_cbranch_vccnz .Lcv_388
	v_lshlrev_b32_e32 v134, 2, v164
	v_lshrrev_b32_e32 v166, 1, v164
	v_and_b32_e32 v167, 0xffffffe3, v164
	v_and_or_b32 v168, v166, 12, v167
	v_and_or_b32 v169, v134, 16, v167
	v_ashrrev_i32_e32 v166, 7, v164
	v_ashrrev_i32_e32 v134, 7, v137
	v_mad_u64_u32 v[166:167], s[20:21], v166, 56, v[134:135]
	v_lshrrev_b32_e32 v134, 3, v169
	v_bfe_u32 v169, v137, 6, 1
	v_ashrrev_i32_e32 v167, 31, v166
	v_and_or_b32 v134, v134, 14, v169
	v_lshlrev_b32_e32 v168, 6, v168
	v_and_b32_e32 v169, 63, v137
	v_lshlrev_b64 v[166:167], 14, v[166:167]
	v_and_or_b32 v168, v168, s68, v169
	v_lshlrev_b32_e32 v134, 10, v134
	v_and_b32_e32 v169, 32, v165
	v_bitop3_b32 v134, v134, v168, v169 bitop3:0xf6
	v_lshl_add_u64 v[166:167], s[6:7], 0, v[166:167]
	v_lshl_add_u64 v[166:167], v[166:167], 0, v[134:135]
	s_mov_b64 s[46:47], 0
	s_waitcnt lgkmcnt(0)
	global_store_dwordx4 v[166:167], v[130:133], off nt

.Lcv_390:
	s_waitcnt lgkmcnt(0)
	ds_read_b128 v[130:133], v163
	v_add_u32_e32 v164, s4, v154
	s_mov_b64 s[46:47], -1
	s_and_b64 vcc, exec, s[2:3]
	v_lshlrev_b32_e32 v165, 1, v164
	s_cbranch_vccnz .Lcv_392
	v_lshlrev_b32_e32 v134, 2, v164
	v_lshrrev_b32_e32 v166, 1, v164
	v_and_b32_e32 v167, 0xffffffe3, v164
	v_and_or_b32 v168, v166, 12, v167
	v_and_or_b32 v169, v134, 16, v167
	v_ashrrev_i32_e32 v166, 7, v164
	v_ashrrev_i32_e32 v134, 7, v137
	v_mad_u64_u32 v[166:167], s[2:3], v166, 56, v[134:135]
	v_lshrrev_b32_e32 v134, 3, v169
	v_bfe_u32 v169, v137, 6, 1
	v_ashrrev_i32_e32 v167, 31, v166
	v_and_or_b32 v134, v134, 14, v169
	v_lshlrev_b32_e32 v168, 6, v168
	v_and_b32_e32 v137, 63, v137
	v_lshlrev_b64 v[166:167], 14, v[166:167]
	v_and_or_b32 v137, v168, s68, v137
	v_lshlrev_b32_e32 v134, 10, v134
	v_and_b32_e32 v168, 32, v165
	v_bitop3_b32 v134, v134, v137, v168 bitop3:0xf6
	v_lshl_add_u64 v[166:167], s[6:7], 0, v[166:167]
	v_lshl_add_u64 v[166:167], v[166:167], 0, v[134:135]
	s_mov_b64 s[46:47], 0
	s_waitcnt lgkmcnt(0)
	global_store_dwordx4 v[166:167], v[130:133], off nt

.Lcv_402:
	ds_write_b128 v142, v[66:69]
	ds_write_b128 v142, v[70:73] offset:8192
	ds_write_b128 v142, v[74:77] offset:16384
	ds_write_b128 v142, v[78:81] offset:24576
	ds_write_b128 v142, v[82:85] offset:32768
	ds_write_b128 v142, v[86:89] offset:40960
	ds_write_b128 v142, v[90:93] offset:49152
	ds_write_b128 v142, v[94:97] offset:57344
	ds_write_b128 v143, v[98:101]
	ds_write_b128 v144, v[102:105]
	ds_write_b128 v145, v[106:109]
	ds_write_b128 v146, v[110:113]
	ds_write_b128 v147, v[114:117]
	ds_write_b128 v148, v[118:121]
	ds_write_b128 v149, v[122:125]
	ds_write_b128 v150, v[126:129]
	s_waitcnt lgkmcnt(0)
	s_barrier
	ds_read2st64_b32 v[130:131], v151 offset1:4
	ds_read2st64_b32 v[132:133], v151 offset0:8 offset1:12
	ds_read2st64_b32 v[164:165], v151 offset0:24 offset1:28
	ds_read2st64_b32 v[166:167], v151 offset0:56 offset1:60
	s_cmp_gt_i32 s69, 1
	s_waitcnt lgkmcnt(3)
	v_mul_f32_e32 v130, 0x43000000, v130
	v_mul_f32_e32 v131, 0x43000000, v131
	s_waitcnt lgkmcnt(2)
	v_mul_f32_e32 v134, 0x43000000, v132
	v_med3_f32 v132, v130, s11, v155
	v_med3_f32 v131, v131, s11, v155
	v_mov_b32_e32 v130, v135
	v_mul_f32_e32 v137, 0x43000000, v133
	v_cvt_pk_fp8_f32 v130, v132, v131
	ds_read2st64_b32 v[132:133], v151 offset0:16 offset1:20
	v_med3_f32 v131, v134, s11, v155
	v_med3_f32 v134, v137, s11, v155
	v_cvt_pk_fp8_f32 v130, v131, v134 op_sel:[0,0,1]
	s_waitcnt lgkmcnt(2)
	v_mul_f32_e32 v134, 0x43000000, v164
	s_waitcnt lgkmcnt(0)
	v_mul_f32_e32 v131, 0x43000000, v132
	v_mul_f32_e32 v132, 0x43000000, v133
	v_med3_f32 v133, v131, s11, v155
	v_med3_f32 v132, v132, s11, v155
	v_mov_b32_e32 v131, v135
	v_cvt_pk_fp8_f32 v131, v133, v132
	ds_read2st64_b32 v[132:133], v151 offset0:32 offset1:36
	v_mul_f32_e32 v137, 0x43000000, v165
	ds_read2st64_b32 v[164:165], v151 offset0:40 offset1:44
	v_med3_f32 v134, v134, s11, v155
	v_med3_f32 v137, v137, s11, v155
	s_waitcnt lgkmcnt(1)
	v_mul_f32_e32 v132, 0x43000000, v132
	v_mul_f32_e32 v133, 0x43000000, v133
	v_cvt_pk_fp8_f32 v131, v134, v137 op_sel:[0,0,1]
	s_waitcnt lgkmcnt(0)
	v_mul_f32_e32 v134, 0x43000000, v164
	v_med3_f32 v164, v132, s11, v155
	v_med3_f32 v133, v133, s11, v155
	v_mov_b32_e32 v132, v135
	v_mul_f32_e32 v137, 0x43000000, v165
	v_cvt_pk_fp8_f32 v132, v164, v133
	ds_read2st64_b32 v[164:165], v151 offset0:48 offset1:52
	v_med3_f32 v133, v134, s11, v155
	v_med3_f32 v134, v137, s11, v155
	v_cvt_pk_fp8_f32 v132, v133, v134 op_sel:[0,0,1]
	v_mul_f32_e32 v137, 0x43000000, v166
	s_waitcnt lgkmcnt(0)
	v_mul_f32_e32 v133, 0x43000000, v164
	v_mul_f32_e32 v134, 0x43000000, v165
	v_med3_f32 v164, v133, s11, v155
	v_med3_f32 v134, v134, s11, v155
	v_mov_b32_e32 v133, v135
	v_cvt_pk_fp8_f32 v133, v164, v134
	ds_read2st64_b32 v[164:165], v151 offset0:64 offset1:68
	v_mul_f32_e32 v168, 0x43000000, v167
	ds_read2st64_b32 v[166:167], v151 offset0:72 offset1:76
	v_med3_f32 v134, v137, s11, v155
	v_med3_f32 v137, v168, s11, v155
	v_cvt_pk_fp8_f32 v133, v134, v137 op_sel:[0,0,1]
	s_waitcnt lgkmcnt(1)
	v_mul_f32_e32 v134, 0x43000000, v164
	v_mul_f32_e32 v137, 0x43000000, v165
	s_waitcnt lgkmcnt(0)
	v_mul_f32_e32 v165, 0x43000000, v166
	v_mul_f32_e32 v170, 0x43000000, v167
	v_med3_f32 v134, v134, s11, v155
	v_med3_f32 v137, v137, s11, v155
	v_mov_b32_e32 v164, v135
	ds_read2st64_b32 v[166:167], v151 offset0:80 offset1:84
	v_cvt_pk_fp8_f32 v164, v134, v137
	ds_read2st64_b32 v[168:169], v151 offset0:88 offset1:92
	v_med3_f32 v134, v165, s11, v155
	v_med3_f32 v137, v170, s11, v155
	v_cvt_pk_fp8_f32 v164, v134, v137 op_sel:[0,0,1]
	s_waitcnt lgkmcnt(1)
	v_mul_f32_e32 v134, 0x43000000, v166
	v_mul_f32_e32 v137, 0x43000000, v167
	s_waitcnt lgkmcnt(0)
	v_mul_f32_e32 v168, 0x43000000, v168
	v_med3_f32 v134, v134, s11, v155
	v_med3_f32 v137, v137, s11, v155
	v_mov_b32_e32 v165, v135
	ds_read2st64_b32 v[166:167], v151 offset0:96 offset1:100
	v_mul_f32_e32 v170, 0x43000000, v169
	v_cvt_pk_fp8_f32 v165, v134, v137
	v_med3_f32 v134, v168, s11, v155
	ds_read2st64_b32 v[168:169], v151 offset0:104 offset1:108
	v_med3_f32 v137, v170, s11, v155
	v_cvt_pk_fp8_f32 v165, v134, v137 op_sel:[0,0,1]
	s_waitcnt lgkmcnt(1)
	v_mul_f32_e32 v134, 0x43000000, v166
	v_mul_f32_e32 v137, 0x43000000, v167
	s_waitcnt lgkmcnt(0)
	v_mul_f32_e32 v167, 0x43000000, v168
	v_mul_f32_e32 v172, 0x43000000, v169
	v_med3_f32 v134, v134, s11, v155
	v_med3_f32 v137, v137, s11, v155
	v_mov_b32_e32 v166, v135
	ds_read2st64_b32 v[168:169], v151 offset0:112 offset1:116
	v_cvt_pk_fp8_f32 v166, v134, v137
	ds_read2st64_b32 v[170:171], v151 offset0:120 offset1:124
	v_med3_f32 v134, v167, s11, v155
	v_med3_f32 v137, v172, s11, v155
	v_cvt_pk_fp8_f32 v166, v134, v137 op_sel:[0,0,1]
	s_waitcnt lgkmcnt(1)
	v_mul_f32_e32 v134, 0x43000000, v168
	v_mul_f32_e32 v137, 0x43000000, v169
	s_waitcnt lgkmcnt(0)
	v_mul_f32_e32 v170, 0x43000000, v170
	v_med3_f32 v134, v134, s11, v155
	v_med3_f32 v137, v137, s11, v155
	v_mov_b32_e32 v167, v135
	ds_read2st64_b32 v[168:169], v151 offset0:128 offset1:132
	v_mul_f32_e32 v172, 0x43000000, v171
	v_cvt_pk_fp8_f32 v167, v134, v137
	v_med3_f32 v134, v170, s11, v155
	ds_read2st64_b32 v[170:171], v151 offset0:136 offset1:140
	v_med3_f32 v137, v172, s11, v155
	v_cvt_pk_fp8_f32 v167, v134, v137 op_sel:[0,0,1]
	s_waitcnt lgkmcnt(1)
	v_mul_f32_e32 v134, 0x43000000, v168
	v_mul_f32_e32 v137, 0x43000000, v169
	s_waitcnt lgkmcnt(0)
	v_mul_f32_e32 v169, 0x43000000, v170
	v_mul_f32_e32 v174, 0x43000000, v171
	v_med3_f32 v134, v134, s11, v155
	v_med3_f32 v137, v137, s11, v155
	v_mov_b32_e32 v168, v135
	ds_read2st64_b32 v[170:171], v151 offset0:144 offset1:148
	v_cvt_pk_fp8_f32 v168, v134, v137
	ds_read2st64_b32 v[172:173], v151 offset0:152 offset1:156
	v_med3_f32 v134, v169, s11, v155
	v_med3_f32 v137, v174, s11, v155
	v_cvt_pk_fp8_f32 v168, v134, v137 op_sel:[0,0,1]
	s_waitcnt lgkmcnt(1)
	v_mul_f32_e32 v134, 0x43000000, v170
	v_mul_f32_e32 v137, 0x43000000, v171
	s_waitcnt lgkmcnt(0)
	v_mul_f32_e32 v172, 0x43000000, v172
	v_med3_f32 v134, v134, s11, v155
	v_med3_f32 v137, v137, s11, v155
	v_mov_b32_e32 v169, v135
	ds_read2st64_b32 v[170:171], v151 offset0:160 offset1:164
	v_mul_f32_e32 v174, 0x43000000, v173
	v_cvt_pk_fp8_f32 v169, v134, v137
	v_med3_f32 v134, v172, s11, v155
	ds_read2st64_b32 v[172:173], v151 offset0:168 offset1:172
	v_med3_f32 v137, v174, s11, v155
	v_cvt_pk_fp8_f32 v169, v134, v137 op_sel:[0,0,1]
	s_waitcnt lgkmcnt(1)
	v_mul_f32_e32 v134, 0x43000000, v170
	v_mul_f32_e32 v137, 0x43000000, v171
	s_waitcnt lgkmcnt(0)
	v_mul_f32_e32 v171, 0x43000000, v172
	v_mul_f32_e32 v176, 0x43000000, v173
	v_med3_f32 v134, v134, s11, v155
	v_med3_f32 v137, v137, s11, v155
	v_mov_b32_e32 v170, v135
	ds_read2st64_b32 v[172:173], v151 offset0:176 offset1:180
	v_cvt_pk_fp8_f32 v170, v134, v137
	ds_read2st64_b32 v[174:175], v151 offset0:184 offset1:188
	v_med3_f32 v134, v171, s11, v155
	v_med3_f32 v137, v176, s11, v155
	v_cvt_pk_fp8_f32 v170, v134, v137 op_sel:[0,0,1]
	s_waitcnt lgkmcnt(1)
	v_mul_f32_e32 v134, 0x43000000, v172
	v_mul_f32_e32 v137, 0x43000000, v173
	s_waitcnt lgkmcnt(0)
	v_mul_f32_e32 v174, 0x43000000, v174
	v_med3_f32 v134, v134, s11, v155
	v_med3_f32 v137, v137, s11, v155
	v_mov_b32_e32 v171, v135
	ds_read2st64_b32 v[172:173], v151 offset0:192 offset1:196
	v_mul_f32_e32 v176, 0x43000000, v175
	v_cvt_pk_fp8_f32 v171, v134, v137
	v_med3_f32 v134, v174, s11, v155
	ds_read2st64_b32 v[174:175], v151 offset0:200 offset1:204
	v_med3_f32 v137, v176, s11, v155
	v_cvt_pk_fp8_f32 v171, v134, v137 op_sel:[0,0,1]
	s_waitcnt lgkmcnt(1)
	v_mul_f32_e32 v134, 0x43000000, v172
	v_mul_f32_e32 v137, 0x43000000, v173
	s_waitcnt lgkmcnt(0)
	v_mul_f32_e32 v173, 0x43000000, v174
	v_mul_f32_e32 v178, 0x43000000, v175
	v_med3_f32 v134, v134, s11, v155
	v_med3_f32 v137, v137, s11, v155
	v_mov_b32_e32 v172, v135
	ds_read2st64_b32 v[174:175], v151 offset0:208 offset1:212
	v_cvt_pk_fp8_f32 v172, v134, v137
	ds_read2st64_b32 v[176:177], v151 offset0:216 offset1:220
	v_med3_f32 v134, v173, s11, v155
	v_med3_f32 v137, v178, s11, v155
	v_cvt_pk_fp8_f32 v172, v134, v137 op_sel:[0,0,1]
	s_waitcnt lgkmcnt(1)
	v_mul_f32_e32 v134, 0x43000000, v174
	v_mul_f32_e32 v137, 0x43000000, v175
	s_waitcnt lgkmcnt(0)
	v_mul_f32_e32 v176, 0x43000000, v176
	v_med3_f32 v134, v134, s11, v155
	v_med3_f32 v137, v137, s11, v155
	v_mov_b32_e32 v173, v135
	ds_read2st64_b32 v[174:175], v151 offset0:224 offset1:228
	v_mul_f32_e32 v178, 0x43000000, v177
	v_cvt_pk_fp8_f32 v173, v134, v137
	v_med3_f32 v134, v176, s11, v155
	ds_read2st64_b32 v[176:177], v151 offset0:232 offset1:236
	v_med3_f32 v137, v178, s11, v155
	v_cvt_pk_fp8_f32 v173, v134, v137 op_sel:[0,0,1]
	s_waitcnt lgkmcnt(1)
	v_mul_f32_e32 v134, 0x43000000, v174
	v_mul_f32_e32 v137, 0x43000000, v175
	s_waitcnt lgkmcnt(0)
	v_mul_f32_e32 v175, 0x43000000, v176
	v_mul_f32_e32 v180, 0x43000000, v177
	v_med3_f32 v134, v134, s11, v155
	v_med3_f32 v137, v137, s11, v155
	v_mov_b32_e32 v174, v135
	ds_read2st64_b32 v[176:177], v151 offset0:240 offset1:244
	v_cvt_pk_fp8_f32 v174, v134, v137
	v_med3_f32 v134, v175, s11, v155
	ds_read2st64_b32 v[178:179], v151 offset0:248 offset1:252
	v_med3_f32 v137, v180, s11, v155
	v_cvt_pk_fp8_f32 v174, v134, v137 op_sel:[0,0,1]
	s_waitcnt lgkmcnt(1)
	v_mul_f32_e32 v134, 0x43000000, v176
	v_mul_f32_e32 v137, 0x43000000, v177
	v_med3_f32 v134, v134, s11, v155
	v_med3_f32 v137, v137, s11, v155
	v_mov_b32_e32 v175, v135
	v_cvt_pk_fp8_f32 v175, v134, v137
	s_waitcnt lgkmcnt(0)
	v_mul_f32_e32 v176, 0x43000000, v178
	v_mul_f32_e32 v134, 0x43000000, v179
	v_med3_f32 v137, v176, s11, v155
	v_med3_f32 v134, v134, s11, v155
	v_cvt_pk_fp8_f32 v175, v137, v134 op_sel:[0,0,1]
	s_barrier
	ds_write_b128 v156, v[130:133]
	ds_write_b128 v157, v[164:167]
	ds_write_b128 v158, v[168:171]
	ds_write_b128 v159, v[172:175]
	s_waitcnt lgkmcnt(0)
	s_barrier
	ds_read_b128 v[130:133], v160
	v_add_u32_e32 v164, s72, v140
	s_cselect_b64 s[44:45], -1, 0
	s_mov_b64 s[2:3], -1
	s_and_b64 vcc, exec, s[44:45]
	v_lshlrev_b32_e32 v165, 1, v164
	v_add_u32_e32 v137, s14, v138
	s_cbranch_vccz .Lcv_404
	v_lshlrev_b32_e32 v134, 2, v164
	v_lshrrev_b32_e32 v166, 1, v164
	v_and_b32_e32 v167, 0xffffffe3, v164
	v_and_or_b32 v168, v166, 12, v167
	v_and_or_b32 v169, v134, 16, v167
	v_ashrrev_i32_e32 v166, 7, v164
	v_ashrrev_i32_e32 v134, 7, v137
	v_mad_u64_u32 v[166:167], s[2:3], v166, 56, v[134:135]
	v_lshrrev_b32_e32 v134, 3, v169
	v_bfe_u32 v169, v137, 6, 1
	v_ashrrev_i32_e32 v167, 31, v166
	v_and_or_b32 v134, v134, 14, v169
	v_lshlrev_b32_e32 v168, 6, v168
	v_and_b32_e32 v169, 63, v137
	v_lshlrev_b64 v[166:167], 14, v[166:167]
	v_and_or_b32 v168, v168, s68, v169
	v_lshlrev_b32_e32 v134, 10, v134
	v_and_b32_e32 v169, 32, v165
	v_bitop3_b32 v134, v134, v168, v169 bitop3:0xf6
	v_lshl_add_u64 v[166:167], s[40:41], 0, v[166:167]
	v_lshl_add_u64 v[166:167], v[166:167], 0, v[134:135]
	s_waitcnt lgkmcnt(0)
	global_store_dwordx4 v[166:167], v[130:133], off nt
	s_mov_b64 s[2:3], 0
.Lcv_404:
	s_andn2_b64 vcc, exec, s[2:3]
	s_cbranch_vccnz .Lcv_406
	s_cmp_eq_u32 s69, 1
	v_and_b32_e32 v134, 0xffffff00, v165
	v_and_b32_e32 v164, 0x7f, v164
	s_cselect_b32 s1, 0x80, 0
	v_or3_b32 v164, v164, s1, v134
	v_ashrrev_i32_e32 v165, 31, v164
	v_lshlrev_b64 v[164:165], 11, v[164:165]
	v_lshl_add_u64 v[164:165], s[40:41], 0, v[164:165]
	s_ashr_i32 s15, s14, 31
	v_lshl_add_u64 v[164:165], v[164:165], 0, s[14:15]
	v_lshl_add_u64 v[164:165], v[164:165], 0, v[138:139]
	s_waitcnt lgkmcnt(0)
	global_store_dwordx4 v[164:165], v[130:133], off nt
.Lcv_406:
	s_waitcnt lgkmcnt(0)
	ds_read_b128 v[130:133], v161
	v_add_u32_e32 v164, s72, v152
	v_cndmask_b32_e64 v134, 0, 1, s[44:45]
	s_mov_b64 s[46:47], -1
	v_cmp_ne_u32_e64 s[2:3], 1, v134
	s_andn2_b64 vcc, exec, s[44:45]
	v_lshlrev_b32_e32 v165, 1, v164
	s_cbranch_vccnz .Lcv_408
	v_lshlrev_b32_e32 v134, 2, v164
	v_lshrrev_b32_e32 v166, 1, v164
	v_and_b32_e32 v167, 0xffffffe3, v164
	v_and_or_b32 v168, v166, 12, v167
	v_and_or_b32 v169, v134, 16, v167
	v_ashrrev_i32_e32 v166, 7, v164
	v_ashrrev_i32_e32 v134, 7, v137
	v_mad_u64_u32 v[166:167], s[20:21], v166, 56, v[134:135]
	v_lshrrev_b32_e32 v134, 3, v169
	v_bfe_u32 v169, v137, 6, 1
	v_ashrrev_i32_e32 v167, 31, v166
	v_and_or_b32 v134, v134, 14, v169
	v_lshlrev_b32_e32 v168, 6, v168
	v_and_b32_e32 v169, 63, v137
	v_lshlrev_b64 v[166:167], 14, v[166:167]
	v_and_or_b32 v168, v168, s68, v169
	v_lshlrev_b32_e32 v134, 10, v134
	v_and_b32_e32 v169, 32, v165
	v_bitop3_b32 v134, v134, v168, v169 bitop3:0xf6
	v_lshl_add_u64 v[166:167], s[40:41], 0, v[166:167]
	v_lshl_add_u64 v[166:167], v[166:167], 0, v[134:135]
	s_mov_b64 s[46:47], 0
	s_waitcnt lgkmcnt(0)
	global_store_dwordx4 v[166:167], v[130:133], off nt
.Lcv_408:
	s_andn2_b64 vcc, exec, s[46:47]
	s_cbranch_vccnz .Lcv_410
	s_cmp_eq_u32 s69, 1
	v_and_b32_e32 v134, 0xffffff00, v165
	v_and_b32_e32 v164, 0x7f, v164
	s_cselect_b32 s1, 0x80, 0
	v_or3_b32 v164, v164, s1, v134
	v_ashrrev_i32_e32 v165, 31, v164
	v_lshlrev_b64 v[164:165], 11, v[164:165]
	v_lshl_add_u64 v[164:165], s[40:41], 0, v[164:165]
	s_ashr_i32 s15, s14, 31
	v_lshl_add_u64 v[164:165], v[164:165], 0, s[14:15]
	v_lshl_add_u64 v[164:165], v[164:165], 0, v[138:139]
	s_waitcnt lgkmcnt(0)
	global_store_dwordx4 v[164:165], v[130:133], off nt
.Lcv_410:
	s_waitcnt lgkmcnt(0)
	ds_read_b128 v[130:133], v162
	v_add_u32_e32 v164, s72, v153
	s_mov_b64 s[44:45], -1
	s_and_b64 vcc, exec, s[2:3]
	v_lshlrev_b32_e32 v165, 1, v164
	s_cbranch_vccnz .Lcv_412
	v_lshlrev_b32_e32 v134, 2, v164
	v_lshrrev_b32_e32 v166, 1, v164
	v_and_b32_e32 v167, 0xffffffe3, v164
	v_and_or_b32 v168, v166, 12, v167
	v_and_or_b32 v169, v134, 16, v167
	v_ashrrev_i32_e32 v166, 7, v164
	v_ashrrev_i32_e32 v134, 7, v137
	v_mad_u64_u32 v[166:167], s[20:21], v166, 56, v[134:135]
	v_lshrrev_b32_e32 v134, 3, v169
	v_bfe_u32 v169, v137, 6, 1
	v_ashrrev_i32_e32 v167, 31, v166
	v_and_or_b32 v134, v134, 14, v169
	v_lshlrev_b32_e32 v168, 6, v168
	v_and_b32_e32 v169, 63, v137
	v_lshlrev_b64 v[166:167], 14, v[166:167]
	v_and_or_b32 v168, v168, s68, v169
	v_lshlrev_b32_e32 v134, 10, v134
	v_and_b32_e32 v169, 32, v165
	v_bitop3_b32 v134, v134, v168, v169 bitop3:0xf6
	v_lshl_add_u64 v[166:167], s[40:41], 0, v[166:167]
	v_lshl_add_u64 v[166:167], v[166:167], 0, v[134:135]
	s_mov_b64 s[44:45], 0
	s_waitcnt lgkmcnt(0)
	global_store_dwordx4 v[166:167], v[130:133], off nt
.Lcv_412:
	s_andn2_b64 vcc, exec, s[44:45]
	s_cbranch_vccnz .Lcv_414
	s_cmp_eq_u32 s69, 1
	v_and_b32_e32 v134, 0xffffff00, v165
	v_and_b32_e32 v164, 0x7f, v164
	s_cselect_b32 s1, 0x80, 0
	v_or3_b32 v164, v164, s1, v134
	v_ashrrev_i32_e32 v165, 31, v164
	v_lshlrev_b64 v[164:165], 11, v[164:165]
	v_lshl_add_u64 v[164:165], s[40:41], 0, v[164:165]
	s_ashr_i32 s15, s14, 31
	v_lshl_add_u64 v[164:165], v[164:165], 0, s[14:15]
	v_lshl_add_u64 v[164:165], v[164:165], 0, v[138:139]
	s_waitcnt lgkmcnt(0)
	global_store_dwordx4 v[164:165], v[130:133], off nt
.Lcv_414:
	s_waitcnt lgkmcnt(0)
	ds_read_b128 v[130:133], v163
	v_add_u32_e32 v164, s72, v154
	s_mov_b64 s[44:45], -1
	s_and_b64 vcc, exec, s[2:3]
	v_lshlrev_b32_e32 v165, 1, v164
	s_cbranch_vccnz .Lcv_416
	v_lshlrev_b32_e32 v134, 2, v164
	v_lshrrev_b32_e32 v166, 1, v164
	v_and_b32_e32 v167, 0xffffffe3, v164
	v_and_or_b32 v168, v166, 12, v167
	v_and_or_b32 v169, v134, 16, v167
	v_ashrrev_i32_e32 v166, 7, v164
	v_ashrrev_i32_e32 v134, 7, v137
	v_mad_u64_u32 v[166:167], s[2:3], v166, 56, v[134:135]
	v_lshrrev_b32_e32 v134, 3, v169
	v_bfe_u32 v169, v137, 6, 1
	v_ashrrev_i32_e32 v167, 31, v166
	v_and_or_b32 v134, v134, 14, v169
	v_lshlrev_b32_e32 v168, 6, v168
	v_and_b32_e32 v137, 63, v137
	v_lshlrev_b64 v[166:167], 14, v[166:167]
	v_and_or_b32 v137, v168, s68, v137
	v_lshlrev_b32_e32 v134, 10, v134
	v_and_b32_e32 v168, 32, v165
	v_bitop3_b32 v134, v134, v137, v168 bitop3:0xf6
	v_lshl_add_u64 v[166:167], s[40:41], 0, v[166:167]
	v_lshl_add_u64 v[166:167], v[166:167], 0, v[134:135]
	s_mov_b64 s[44:45], 0
	s_waitcnt lgkmcnt(0)
	global_store_dwordx4 v[166:167], v[130:133], off nt
.Lcv_416:
	s_andn2_b64 vcc, exec, s[44:45]
	s_cbranch_vccnz .Lcv_368
	s_cmp_eq_u32 s69, 1
	v_and_b32_e32 v134, 0xffffff00, v165
	v_and_b32_e32 v137, 0x7f, v164
	s_cselect_b32 s1, 0x80, 0
	v_or3_b32 v164, v137, s1, v134
	v_ashrrev_i32_e32 v165, 31, v164
	v_lshlrev_b64 v[164:165], 11, v[164:165]
	v_lshl_add_u64 v[164:165], s[40:41], 0, v[164:165]
	s_ashr_i32 s15, s14, 31
	v_lshl_add_u64 v[164:165], v[164:165], 0, s[14:15]
	v_lshl_add_u64 v[164:165], v[164:165], 0, v[138:139]
	s_waitcnt lgkmcnt(0)
	global_store_dwordx4 v[164:165], v[130:133], off nt
	s_branch .Lcv_368
.Lcv_exit:
	s_mov_b32 s12, s98
	s_branch .LBB0_867

.LBB0_867:
	s_mov_b32 s13, s99
	s_cmp_lt_i32 s59, 9
	s_cbranch_scc1 .LBB0_921
	s_waitcnt vmcnt(0)
	s_waitcnt lgkmcnt(0)
	s_barrier
	s_mov_b64 s[0:1], exec
	v_readlane_b32 s2, v251, 9
	v_readlane_b32 s3, v251, 10
	s_and_b64 s[2:3], s[0:1], s[2:3]
	s_mov_b64 exec, s[2:3]
	s_cbranch_execz .LBB0_920
	s_add_i32 s2, 0, 0x21420
	v_mov_b32_e32 v2, s2
	s_waitcnt vmcnt(0) expcnt(0) lgkmcnt(0)
	ds_read_b32 v4, v2
	s_add_i32 s2, 0, 0x21424
	v_mov_b32_e32 v2, s2
	ds_read_b32 v2, v2
	s_waitcnt lgkmcnt(1)
	v_cmp_ne_u32_e32 vcc, 0, v4
	s_cbranch_vccnz .LBB0_884
	s_load_dwordx2 s[6:7], s[94:95], 0x4
	s_add_u32 s2, s56, 0x4200
	s_addc_u32 s3, s57, 0
	s_add_u32 s4, s56, 0x4400
	s_addc_u32 s5, s57, 0
	s_waitcnt lgkmcnt(0)
	s_mul_i32 s10, s6, s13
	s_add_u32 s6, s56, 0x4500
	s_mul_i32 s10, s10, s7
	s_addc_u32 s7, s57, 0
	s_add_u32 s8, s56, 0x4600
	s_addc_u32 s9, s57, 0
	s_add_u32 s14, s56, 0x4700
	s_addc_u32 s15, s57, 0
	s_add_u32 s26, s56, 0x4800
	s_addc_u32 s27, s57, 0
	s_add_u32 s28, s56, 0x4900
	s_addc_u32 s29, s57, 0
	s_add_u32 s30, s56, 0x4a00
	s_addc_u32 s31, s57, 0
	s_add_u32 s40, s56, 0x4b00
	s_addc_u32 s41, s57, 0
	s_add_u32 s42, s56, 0x4c00
	s_addc_u32 s43, s57, 0
	s_add_u32 s44, s56, 0x4d00
	s_addc_u32 s45, s57, 0
	s_add_u32 s46, s56, 0x4e00
	s_addc_u32 s47, s57, 0
	s_add_u32 s48, s56, 0x4f00
	s_addc_u32 s49, s57, 0
	s_add_u32 s50, s56, 0x5000
	s_addc_u32 s51, s57, 0
	s_add_u32 s52, s56, 0x5100
	s_addc_u32 s53, s57, 0
	s_add_u32 s64, s56, 0x5200
	s_addc_u32 s65, s57, 0
	s_add_u32 s66, s56, 0x5300
	s_addc_u32 s67, s57, 0
	s_mov_b32 s11, 1
	v_mov_b32_e32 v18, 0
	s_branch .LBB0_872

	.amdhsa_kernel _Z10fwd_kernel4Args
		.amdhsa_group_segment_fixed_size 0
		.amdhsa_private_segment_fixed_size 0
		.amdhsa_kernarg_size 448
		.amdhsa_user_sgpr_count 2
		.amdhsa_user_sgpr_dispatch_ptr 0
		.amdhsa_user_sgpr_queue_ptr 0
		.amdhsa_user_sgpr_kernarg_segment_ptr 1
		.amdhsa_user_sgpr_dispatch_id 0
		.amdhsa_user_sgpr_kernarg_preload_length 0
		.amdhsa_user_sgpr_kernarg_preload_offset 0
		.amdhsa_user_sgpr_private_segment_size 0
		.amdhsa_uses_dynamic_stack 0
		.amdhsa_enable_private_segment 0
		.amdhsa_system_sgpr_workgroup_id_x 1
		.amdhsa_system_sgpr_workgroup_id_y 0
		.amdhsa_system_sgpr_workgroup_id_z 0
		.amdhsa_system_sgpr_workgroup_info 0
		.amdhsa_system_vgpr_workitem_id 0
		.amdhsa_next_free_vgpr 252
		.amdhsa_next_free_sgpr 102
		.amdhsa_accum_offset 252
		.amdhsa_reserve_vcc 1
		.amdhsa_float_round_mode_32 0
		.amdhsa_float_round_mode_16_64 0
		.amdhsa_float_denorm_mode_32 3
		.amdhsa_float_denorm_mode_16_64 3
		.amdhsa_dx10_clamp 1
		.amdhsa_ieee_mode 1
		.amdhsa_fp16_overflow 0
		.amdhsa_tg_split 0
		.amdhsa_exception_fp_ieee_invalid_op 0
		.amdhsa_exception_fp_denorm_src 0
		.amdhsa_exception_fp_ieee_div_zero 0
		.amdhsa_exception_fp_ieee_overflow 0
		.amdhsa_exception_fp_ieee_underflow 0
		.amdhsa_exception_fp_ieee_inexact 0
		.amdhsa_exception_int_div_zero 0
	.end_amdhsa_kernel

amdhsa.kernels:
  - .agpr_count:     0
    .args:
      - .offset:         0
        .size:           192
        .value_kind:     by_value
      - .offset:         192
        .size:           4
        .value_kind:     hidden_block_count_x
      - .offset:         196
        .size:           4
        .value_kind:     hidden_block_count_y
      - .offset:         200
        .size:           4
        .value_kind:     hidden_block_count_z
      - .offset:         204
        .size:           2
        .value_kind:     hidden_group_size_x
      - .offset:         206
        .size:           2
        .value_kind:     hidden_group_size_y
      - .offset:         208
        .size:           2
        .value_kind:     hidden_group_size_z
      - .offset:         210
        .size:           2
        .value_kind:     hidden_remainder_x
      - .offset:         212
        .size:           2
        .value_kind:     hidden_remainder_y
      - .offset:         214
        .size:           2
        .value_kind:     hidden_remainder_z
      - .offset:         232
        .size:           8
        .value_kind:     hidden_global_offset_x
      - .offset:         240
        .size:           8
        .value_kind:     hidden_global_offset_y
      - .offset:         248
        .size:           8
        .value_kind:     hidden_global_offset_z
      - .offset:         256
        .size:           2
        .value_kind:     hidden_grid_dims
      - .offset:         312
        .size:           4
        .value_kind:     hidden_dynamic_lds_size
    .group_segment_fixed_size: 0
    .kernarg_segment_align: 8
    .kernarg_segment_size: 448
    .language:       OpenCL C
    .language_version:
      - 2
      - 0
    .max_flat_workgroup_size: 512
    .name:           _Z10fwd_kernel4Args
    .private_segment_fixed_size: 0
    .sgpr_count:     108
    .sgpr_spill_count: 81
    .symbol:         _Z10fwd_kernel4Args.kd
    .uniform_work_group_size: 1
    .uses_dynamic_stack: false
    .vgpr_count:     252
    .vgpr_spill_count: 0
    .wavefront_size: 64
